# final plus non-temporal policy on the attention K/V tile loads
# baseline (speedup 1.0000x reference)
; DI const float* inp(kptr_t k, int i) { return (const float*)k[i]; }
; DI void refresh(Frame& F) { int w = F.wave; unsigned ones_ = ~0u; asm volatile("" : "+s"(w), "+s"(ones_)); int ln = (int)__builtin_amdgcn_mbcnt_hi(ones_, __builtin_amdgcn_mbcnt_lo(ones_, 0u)); asm volatile("" : "+v"(ln)); F.tid = w * 64 + ln; F.lane = ln; F.wave = w; int b = blockIdx.x; asm volatile("" : "+s"(b)); F.bid = b; }
; DI void phase_attn(Frame& F, int l) {
;     ...
;         refresh(F);
;         const int lane = F.lane, wave = F.wave, qi = lane & 31, hh = lane >> 5;
;         const int srow = F.tid >> 3, sch = F.tid & 7;
;         const int c = U & 255, it = U >> 8, bh = c >> 1, set = c & 1;
;         const int qblk = set ? (it == 0 ? 6 : (it == 1 ? 1 : (it == 2 ? 5 : 2))) : (it == 0 ? 7 : (it == 1 ? 0 : (it == 2 ? 4 : 3)));
;         const int b = bh >> 3, h = bh & 7;
;         const size_t qtok = (size_t)b * SEQ + qblk * 256 + 32 * wave + qi;
;         bf16x8 qf[4];
; #pragma unroll
;         for (int s = 0; s < 4; ++s) qf[s] = *(const bf16x8*)(qb + qtok * AW + h * HD + 16 * s + 8 * hh);
;         u32x4 kreg, vreg;
;         { const size_t tok = (size_t)b * SEQ + qblk * 256 + srow; kreg = *(const u32x4*)(kb + tok * AW + h * HD + sch * 8); vreg = *(const u32x4*)(vb + tok * AW + h * HD + sch * 8); }
;         const float km_v = kmean[((size_t)(b * NBLK + (F.tid >> 6))) * AW + h * HD + (F.tid & 63)] * (1.0f / 256.0f);
;         const float bias_v = inp(KA, I_RELB)[t5_bucket(F.tid & 127) * NH + h] * LOG2E;
.LBB0_479:
	s_bfe_u32 s4, s51, 0x40004
	s_lshl_b32 s16, s4, 11
	s_lshl_b32 s2, s37, 8
	s_lshl_b32 s36, s97, 5
	s_lshl_b32 s0, s97, 6
	s_bfe_u32 s1, s51, 0x30001
	s_add_i32 s58, s2, s16
	s_ashr_i32 s2, s36, 31
	s_add_u32 s3, s58, s36
	v_and_b32_e32 v188, 31, v186
	s_addc_u32 s2, 0, s2
	s_waitcnt vmcnt(0)
	v_or_b32_e32 v2, s3, v188
	v_mov_b32_e32 v3, s2
	v_readlane_b32 s2, v253, 19
	v_ashrrev_i32_e32 v16, 5, v186
	v_lshlrev_b64 v[170:171], 10, v[2:3]
	v_readlane_b32 s3, v253, 20
	v_add_u32_e32 v17, s0, v186
	v_lshlrev_b32_e32 v168, 3, v16
	v_lshl_add_u64 v[2:3], s[2:3], 0, v[170:171]
	s_lshl_b32 s2, s1, 7
	s_mov_b32 s3, s59
	v_ashrrev_i32_e32 v10, 3, v17
	v_lshl_add_u64 v[2:3], v[2:3], 0, s[2:3]
	v_ashrrev_i32_e32 v169, 31, v168
	v_lshl_add_u64 v[2:3], v[168:169], 1, v[2:3]
	v_ashrrev_i32_e32 v11, 31, v10
	v_ashrrev_i32_e32 v19, 6, v17
	global_load_dwordx4 v[156:159], v[2:3], off
	global_load_dwordx4 v[152:155], v[2:3], off offset:32
	global_load_dwordx4 v[148:151], v[2:3], off offset:64
	global_load_dwordx4 v[144:147], v[2:3], off offset:96
	v_lshl_add_u64 v[2:3], s[58:59], 0, v[10:11]
	v_readlane_b32 s8, v253, 31
	v_lshl_add_u32 v20, s4, 3, v19
	v_lshlrev_b64 v[2:3], 10, v[2:3]
	v_readlane_b32 s9, v253, 32
	v_ashrrev_i32_e32 v21, 31, v20
	v_and_b32_e32 v19, 63, v186
	v_lshl_add_u64 v[14:15], s[8:9], 0, v[2:3]
	v_readlane_b32 s8, v253, 15
	v_lshlrev_b64 v[20:21], 11, v[20:21]
	v_and_b32_e32 v18, 7, v186
	v_readlane_b32 s9, v253, 16
	v_lshl_add_u64 v[20:21], s[34:35], 0, v[20:21]
	v_lshlrev_b32_e32 v22, 2, v19
	v_mov_b32_e32 v23, v1
	v_lshl_add_u64 v[4:5], v[14:15], 0, s[2:3]
	v_lshlrev_b32_e32 v0, 4, v18
	v_lshl_add_u64 v[12:13], s[8:9], 0, v[2:3]
	v_lshl_add_u64 v[20:21], v[20:21], 0, v[22:23]
	s_lshl_b32 s58, s1, 8
	v_lshl_add_u64 v[178:179], v[4:5], 0, v[0:1]
	v_lshl_add_u64 v[2:3], v[12:13], 0, s[2:3]
	v_lshl_add_u64 v[20:21], v[20:21], 0, s[58:59]
	v_lshl_add_u64 v[180:181], v[2:3], 0, v[0:1]
	global_load_dwordx4 v[2:5], v[178:179], off nt
	global_load_dwordx4 v[6:9], v[180:181], off nt
	global_load_dword v19, v[20:21], off
	v_and_b32_e32 v20, 0x7f, v17
	v_cmp_lt_u32_e32 vcc, 15, v20
	s_and_saveexec_b64 s[2:3], vcc
	s_cbranch_execz .LBB0_481
	v_cmp_lt_u32_e32 vcc, 18, v20
	s_movk_i32 s4, 0x42
	s_nop 0
	v_cndmask_b32_e64 v21, 16, 17, vcc
	v_cmp_lt_u32_e32 vcc, 20, v20
	s_nop 1
	v_cndmask_b32_e64 v22, 0, 1, vcc
	v_cmp_lt_u32_e32 vcc, 23, v20
	s_nop 1
	v_addc_co_u32_e32 v21, vcc, v21, v22, vcc
	v_cmp_lt_u32_e32 vcc, 26, v20
	s_nop 1
	v_cndmask_b32_e64 v22, 0, 1, vcc
	v_cmp_lt_u32_e32 vcc, 30, v20
	s_nop 1
	v_addc_co_u32_e32 v21, vcc, v21, v22, vcc
	v_cmp_lt_u32_e32 vcc, 34, v20
	s_nop 1
	v_cndmask_b32_e64 v22, 0, 1, vcc
	v_cmp_lt_u32_e32 vcc, 39, v20
	s_nop 1
	v_addc_co_u32_e32 v21, vcc, v21, v22, vcc
	v_cmp_lt_u32_e32 vcc, 45, v20
	s_nop 1
	v_cndmask_b32_e64 v22, 0, 1, vcc
	v_cmp_lt_u32_e32 vcc, 51, v20
	s_nop 1
	v_addc_co_u32_e32 v21, vcc, v21, v22, vcc
	v_cmp_lt_u32_e32 vcc, 58, v20
	s_nop 1
	v_cndmask_b32_e64 v22, 0, 1, vcc
	v_cmp_lt_u32_e32 vcc, s4, v20
	s_movk_i32 s4, 0x4c
	s_nop 0
	v_addc_co_u32_e32 v21, vcc, v21, v22, vcc
	v_cmp_lt_u32_e32 vcc, s4, v20
	s_movk_i32 s4, 0x56
	s_nop 0
	v_cndmask_b32_e64 v22, 0, 1, vcc
	v_cmp_lt_u32_e32 vcc, s4, v20
	s_movk_i32 s4, 0x62
	s_nop 0
	v_addc_co_u32_e32 v21, vcc, v21, v22, vcc
	v_cmp_lt_u32_e32 vcc, s4, v20
	s_movk_i32 s4, 0x70
	s_nop 0
	v_cndmask_b32_e64 v22, 0, 1, vcc
	v_cmp_lt_u32_e32 vcc, s4, v20
	s_nop 1
	v_addc_co_u32_e32 v20, vcc, v21, v22, vcc

; #define LAS __attribute__((address_space(3)))
; DI void phase_attn(Frame& F, int l) {
;     ...
;         __syncthreads();
;         if (F.tid < 128) BIAS[F.tid] = bias_v;
;         if (F.tid == 0) OVF[0] = 0;
;         KM[F.tid] = km_v;
;         *(LAS u32x4*)(KS + srow * 144 + sch * 16) = kreg; *(LAS u32x4*)(VS + srow * 144 + sch * 16) = vreg;
;         { const size_t tok = (size_t)b * SEQ + qblk * 256 + 64 + srow; kreg = *(const u32x4*)(kb + tok * AW + h * HD + sch * 8); vreg = *(const u32x4*)(vb + tok * AW + h * HD + sch * 8); }
;         __syncthreads();
.LBB0_483:
	s_or_b64 exec, exec, s[2:3]
	v_cmp_eq_u32_e32 vcc, 0, v17
	s_and_saveexec_b64 s[2:3], vcc
	ds_write_b32 v1, v1 offset:39424
	s_or_b64 exec, exec, s[2:3]
	s_lshl_b32 s58, s1, 6
	s_waitcnt vmcnt(1)
	v_mul_f32_e32 v19, 0x3b800000, v19
	s_movk_i32 s1, 0x90
	ds_write_b32 v20, v19 offset:37376
	v_mul_lo_u32 v19, v10, s1
	v_lshlrev_b32_e32 v18, 3, v18
	v_add3_u32 v189, 0, v19, v0
	s_lshl_b32 s28, s58, 1
	s_mov_b32 s29, s59
	ds_write_b128 v189, v[2:5]
	ds_write_b128 v189, v[6:9] offset:18432
	v_lshl_add_u64 v[2:3], v[14:15], 0, s[28:29]
	v_lshlrev_b32_e32 v0, 1, v18
	v_lshl_add_u64 v[2:3], v[2:3], 0, v[0:1]
	s_mov_b32 s1, 0x10000
	v_add_co_u32_e32 v4, vcc, s1, v2
	s_movk_i32 s1, 0x460
	s_nop 0
	v_addc_co_u32_e32 v5, vcc, 0, v3, vcc
	global_load_dwordx4 v[160:163], v[4:5], off nt
	v_lshl_add_u64 v[4:5], v[12:13], 0, s[28:29]
	v_lshl_add_u64 v[4:5], v[4:5], 0, v[0:1]
	v_add_co_u32_e32 v6, vcc, 0x10000, v4
	s_nop 1
	v_addc_co_u32_e32 v7, vcc, 0, v5, vcc
	global_load_dwordx4 v[164:167], v[6:7], off nt
	v_cmp_gt_i32_e32 vcc, s1, v17
	s_waitcnt lgkmcnt(0)
	s_barrier
	s_and_saveexec_b64 s[2:3], vcc
	s_cbranch_execz .LBB0_490
	s_lshl_b32 s1, s97, 8
	s_add_i32 s1, s1, 0
	s_add_i32 s1, s1, 0x9a40
	v_add_u32_e32 v7, s0, v186
	v_lshl_add_u32 v6, v186, 2, s1
	v_sub_u32_e32 v7, 0xd0, v7
	s_mov_b64 s[4:5], 0
	s_branch .LBB0_488

.LBB0_504:
	s_bitcmp1_b32 s0, 0
	s_cselect_b32 s1, 0x2400, 0
	v_add_u32_e32 v0, s1, v189
	s_add_i32 s1, s33, 2
	s_cmp_ge_u32 s1, s29
	s_waitcnt vmcnt(1)
	ds_write_b128 v0, v[160:163]
	s_waitcnt vmcnt(0)
	ds_write_b128 v0, v[164:167] offset:18432
	s_cbranch_scc1 .LBB0_506
	v_sub_co_u32_e64 v0, s[2:3], s33, 2
	s_nop 0
	v_readfirstlane_b32 s6, v0
	s_not_b32 s6, s6
	s_lshr_b32 s10, s6, 2
	s_and_b64 s[6:7], s[2:3], exec
	s_cselect_b32 s6, 0, s10
	s_add_i32 s6, s6, s37
	s_lshl_b32 s10, s6, 8
	s_ashr_i32 s11, s10, 31
	s_sub_i32 s17, 5, s33
	s_and_b64 s[6:7], s[8:9], exec
	s_cselect_b32 s6, s17, s16
	s_and_b64 s[2:3], s[2:3], exec
	s_cselect_b32 s1, s1, s6
	s_lshl_b32 s1, s1, 6
	s_ashr_i32 s3, s1, 31
	s_add_u32 s2, s10, s1
	s_addc_u32 s3, s11, s3
	v_lshl_add_u64 v[2:3], s[2:3], 0, v[176:177]
	v_lshlrev_b64 v[2:3], 10, v[2:3]
	v_lshl_add_u64 v[4:5], v[172:173], 0, v[2:3]
	v_lshl_add_u64 v[2:3], v[174:175], 0, v[2:3]
	global_load_dwordx4 v[160:163], v[4:5], off nt
	global_load_dwordx4 v[164:167], v[2:3], off nt

.LBB0_511:
	s_add_i32 s1, s38, 1
	s_cmp_ge_u32 s1, s29
	s_cselect_b64 s[2:3], -1, 0
	s_and_b64 vcc, exec, s[2:3]
	s_cbranch_vccnz .LBB0_514
	s_bitcmp1_b32 s1, 0
	s_cselect_b32 s4, 0x2400, 0
	v_add_u32_e32 v0, s4, v189
	s_add_i32 s4, s38, 2
	s_cmp_ge_u32 s4, s29
	s_waitcnt vmcnt(1)
	ds_write_b128 v0, v[160:163]
	s_waitcnt vmcnt(0)
	ds_write_b128 v0, v[164:167] offset:18432
	s_cbranch_scc1 .LBB0_514
	s_add_i32 s5, s38, -2
	s_not_b32 s5, s5
	s_lshr_b32 s5, s5, 2
	s_add_i32 s5, s37, s5
	s_lshl_b32 s5, s5, 8
	s_ashr_i32 s6, s5, 31
	s_and_b32 s4, s4, 3
	s_cmp_lt_u32 s38, 6
	s_cselect_b32 s0, s0, s4
	s_lshl_b32 s0, s0, 6
	s_add_u32 s4, s0, s5
	s_addc_u32 s5, 0, s6
	v_lshl_add_u64 v[2:3], s[4:5], 0, v[176:177]
	v_lshlrev_b64 v[2:3], 10, v[2:3]
	v_lshl_add_u64 v[4:5], v[172:173], 0, v[2:3]
	v_lshl_add_u64 v[2:3], v[174:175], 0, v[2:3]
	global_load_dwordx4 v[160:163], v[4:5], off nt
	global_load_dwordx4 v[164:167], v[2:3], off nt
